# expert-up: skip MFMA clusters whose 64-row block is all padding rows (rstd==0 flags prefetched per tile)
# speedup vs baseline: 1.0029x; 1.0029x over previous
; #define PG8_STAGE(bufoff, gbase, voff) do { _Pragma("unroll") for (int _i = 0; _i < 2; ++_i) \
;         __builtin_amdgcn_global_load_lds((const unsigned*)((const char*)(gbase) + (voff)[_i]), (LAS unsigned*)(lds + (bufoff) + ldsw + _i * 8192), 16, 0, 0); } while (0)
; #define PG8_WAIT_V(n) asm volatile("s_waitcnt vmcnt(" #n ")" ::: "memory")
; #define PG8_BAR __builtin_amdgcn_s_barrier()
;     ...
;     Unit cur, nxt; int ui = 0;
;     if (!S.next(0, cur)) return;
;     f32x4 acc[2][2][4][2];
; #pragma unroll
;     for (int a = 0; a < 2; ++a)
; #pragma unroll
;         for (int b = 0; b < 2; ++b)
; #pragma unroll
;             for (int m = 0; m < 4; ++m)
; #pragma unroll
;                 for (int n = 0; n < 2; ++n) acc[a][b][m][n] = (f32x4){0.f, 0.f, 0.f, 0.f};
;     i32x8 At[4], B0[2], B1[2];
;     const char* cA = cur.A; const char* cB = cur.B;
;     if constexpr (SP2) {
;         PG8_STAGE(PG8_SB(0, 0), cB, voffB); PG8_STAGE(PG8_SB(0, 1), cB + hstep, voffB); PG8_STAGE(PG8_SA(0, 0), cA, voffA); PG8_STAGE(PG8_SA(0, 1), cA + hstep, voffA);
;         if (wr == 1) PG8_BAR;
;         PG8_WAIT_V(2); PG8_BAR;
;         PG8_STAGE(PG8_SB(1, 0), cB + kstep, voffB); PG8_STAGE(PG8_SA(1, 0), cA + kstep, voffA); PG8_STAGE(PG8_SB(1, 1), cB + hstep + kstep, voffB);
;         PG8_WAIT_V(6); PG8_BAR;
;     __device__ __forceinline__ bool next(int i, pg8::Unit& u) const {
;         const int T = tiles[0]; const long Lx = (long)i * G + c; if (Lx >= (long)T * nN) return false;
;         pg8::tile_of((int)Lx, T, nN, u.pm, u.pn); const int e = tiles[1 + u.pm]; u.z = e;
;         u.A = A0 + (size_t)u.pm * tsA; u.B = B0 + (size_t)e * estride + (size_t)u.pn * tsB; return true;
;     }
.LBB0_2249:
	s_movk_i32 s0, 0x800
	v_mov_b32_e32 v163, 0
	global_load_dword v1, v163, s[10:11]
	s_ashr_i32 s3, s2, 31
	v_readfirstlane_b32 s4, v0
	s_waitcnt vmcnt(0) lgkmcnt(0)
	v_mul_hi_i32 v3, v1, 56
	v_mul_lo_u32 v2, v1, 56
	v_cmp_ge_i64_e32 vcc, s[2:3], v[2:3]
	v_readfirstlane_b32 s1, v1
	s_cbranch_vccnz .LBB0_2266
	v_and_b32_e32 v248, 63, v0
	v_lshlrev_b32_e32 v249, 2, v248
	global_load_dword v250, v249, s[10:11] offset:4
	global_load_dword v251, v249, s[10:11] offset:260
	v_add_u32_e32 v252, 64, v248
	s_mov_b32 s100, 0
	s_mov_b32 s101, 0
	s_waitcnt vmcnt(0)
	v_cmp_gt_u32_e32 vcc, s1, v248
	s_nop 1
	v_cndmask_b32_e32 v250, 8, v250, vcc
	v_cmp_gt_u32_e32 vcc, s1, v252
	s_nop 1
	v_cndmask_b32_e32 v251, 8, v251, vcc
	v_cmp_gt_u32_e32 vcc, 1, v250
	s_bcnt1_i32_b64 s20, vcc
	v_cmp_gt_u32_e32 vcc, 1, v251
	s_bcnt1_i32_b64 s21, vcc
	s_add_u32 s20, s20, s21
	s_mov_b32 s21, 0
	s_or_b64 s[100:101], s[100:101], s[20:21]
	v_cmp_gt_u32_e32 vcc, 2, v250
	s_bcnt1_i32_b64 s20, vcc
	v_cmp_gt_u32_e32 vcc, 2, v251
	s_bcnt1_i32_b64 s21, vcc
	s_add_u32 s20, s20, s21
	s_mov_b32 s21, 0
	s_lshl_b64 s[20:21], s[20:21], 7
	s_or_b64 s[100:101], s[100:101], s[20:21]
	v_cmp_gt_u32_e32 vcc, 3, v250
	s_bcnt1_i32_b64 s20, vcc
	v_cmp_gt_u32_e32 vcc, 3, v251
	s_bcnt1_i32_b64 s21, vcc
	s_add_u32 s20, s20, s21
	s_mov_b32 s21, 0
	s_lshl_b64 s[20:21], s[20:21], 14
	s_or_b64 s[100:101], s[100:101], s[20:21]
	v_cmp_gt_u32_e32 vcc, 4, v250
	s_bcnt1_i32_b64 s20, vcc
	v_cmp_gt_u32_e32 vcc, 4, v251
	s_bcnt1_i32_b64 s21, vcc
	s_add_u32 s20, s20, s21
	s_mov_b32 s21, 0
	s_lshl_b64 s[20:21], s[20:21], 21
	s_or_b64 s[100:101], s[100:101], s[20:21]
	v_cmp_gt_u32_e32 vcc, 5, v250
	s_bcnt1_i32_b64 s20, vcc
	v_cmp_gt_u32_e32 vcc, 5, v251
	s_bcnt1_i32_b64 s21, vcc
	s_add_u32 s20, s20, s21
	s_mov_b32 s21, 0
	s_lshl_b64 s[20:21], s[20:21], 28
	s_or_b64 s[100:101], s[100:101], s[20:21]
	v_cmp_gt_u32_e32 vcc, 6, v250
	s_bcnt1_i32_b64 s20, vcc
	v_cmp_gt_u32_e32 vcc, 6, v251
	s_bcnt1_i32_b64 s21, vcc
	s_add_u32 s20, s20, s21
	s_mov_b32 s21, 0
	s_lshl_b64 s[20:21], s[20:21], 35
	s_or_b64 s[100:101], s[100:101], s[20:21]
	v_cmp_gt_u32_e32 vcc, 7, v250
	s_bcnt1_i32_b64 s20, vcc
	v_cmp_gt_u32_e32 vcc, 7, v251
	s_bcnt1_i32_b64 s21, vcc
	s_add_u32 s20, s20, s21
	s_mov_b32 s21, 0
	s_lshl_b64 s[20:21], s[20:21], 42
	s_or_b64 s[100:101], s[100:101], s[20:21]
	s_mov_b32 s20, s1
	s_mov_b32 s21, 0
	s_lshl_b64 s[20:21], s[20:21], 49
	s_or_b64 s[100:101], s[100:101], s[20:21]
	s_add_u32 s16, s52, 0xde00000
	s_addc_u32 s17, s53, 0
	s_lshr_b32 s21, s3, 29
	s_add_i32 s21, s2, s21
	s_and_b32 s22, s21, -8
	s_sub_i32 s22, s2, s22
	s_mul_i32 s20, s1, 7
	s_lshr_b32 s23, s22, 31
	s_add_i32 s20, s20, s23
	s_mul_i32 s20, s20, s22
	s_ashr_i32 s21, s21, 3
	s_add_i32 s22, s20, s21
	s_mul_hi_i32 s20, s22, 0x92492493
	s_add_i32 s20, s20, s22
	s_lshr_b32 s21, s20, 31
	s_ashr_i32 s20, s20, 8
	s_add_i32 s23, s20, s21
	s_lshl_b32 s24, s23, 3
	s_sub_i32 s1, s1, s24
	s_min_i32 s25, s1, 8
	s_abs_i32 s29, s25
	v_cvt_f32_u32_e32 v1, s29
	s_sub_i32 s36, 0, s29
	s_mulk_i32 s23, 0x1c0
	s_sub_i32 s22, s22, s23
	v_rcp_iflag_f32_e32 v1, v1
	s_abs_i32 s35, s22
	s_lshr_b32 s5, s4, 6
	s_ashr_i32 s1, s0, 31
	v_mul_f32_e32 v1, 0x4f7ffffe, v1
	v_cvt_u32_f32_e32 v1, v1
	s_xor_b32 s23, s22, s25
	s_lshr_b32 s28, s4, 8
	s_lshl_b64 s[20:21], s[0:1], 7
	v_readfirstlane_b32 s37, v1
	s_mul_i32 s36, s36, s37
	s_mul_hi_u32 s36, s37, s36
	s_add_i32 s37, s37, s36
	s_mul_hi_u32 s36, s35, s37
	s_mul_i32 s37, s36, s29
	s_sub_i32 s35, s35, s37
	s_lshl_b32 s34, s5, 10
	s_ashr_i32 s23, s23, 31
	s_add_i32 s37, s36, 1
	s_sub_i32 s38, s35, s29
	s_cmp_ge_u32 s35, s29
	s_cselect_b32 s36, s37, s36
	s_cselect_b32 s35, s38, s35
	s_add_i32 s37, s36, 1
	s_cmp_ge_u32 s35, s29
	s_cselect_b32 s29, s37, s36
	s_xor_b32 s29, s29, s23
	s_sub_i32 s48, s29, s23
	s_mul_i32 s23, s48, s25
	s_sub_i32 s22, s22, s23
	s_add_i32 s62, s24, s22
	s_ashr_i32 s63, s62, 31
	s_lshl_b64 s[22:23], s[62:63], 2
	s_add_u32 s22, s10, s22
	s_addc_u32 s23, s11, s23
	global_load_dword v1, v163, s[22:23] offset:4
	v_lshrrev_b32_e32 v254, 8, v0
	v_lshlrev_b32_e32 v254, 6, v254
	v_lshl_add_u32 v254, s62, 8, v254
	v_lshlrev_b32_e32 v254, 2, v254
	global_load_dword v255, v254, s[14:15] offset:512
	global_load_dword v254, v254, s[14:15]
	v_lshlrev_b32_e32 v2, 4, v0
	v_lshrrev_b32_e32 v3, 3, v0
	s_movk_i32 s22, 0x70
	v_and_b32_e32 v4, 32, v0
	v_bfe_u32 v16, v0, 2, 4
	v_and_b32_e32 v17, 64, v0
	v_bitop3_b32 v19, v3, s22, 64 bitop3:0xc8
	v_bitop3_b32 v18, v2, v4, 48 bitop3:0x6c
	v_and_b32_e32 v20, 48, v3
	v_or_b32_e32 v3, v19, v16
	v_or_b32_e32 v2, v18, v17
	v_or_b32_e32 v4, v20, v16
	v_mad_u64_u32 v[164:165], s[22:23], s0, v3, v[2:3]
	v_mad_u64_u32 v[4:5], s[22:23], s0, v4, v[2:3]
	s_lshl_b64 s[22:23], s[62:63], 19
	s_mov_b32 s35, 0x3800000
	s_add_u32 s64, s42, s22
	s_addc_u32 s65, s43, s23
	s_ashr_i32 s49, s48, 31
	s_lshl_b64 s[22:23], s[48:49], 19
	s_add_i32 s44, s34, 0
	s_add_i32 m0, s44, 0x10000
	s_add_i32 s45, s44, 0x2000
	v_mov_b32_e32 v162, v4
	v_mov_b32_e32 v165, v163
	s_mov_b32 s51, 0
	v_lshl_add_u64 v[10:11], s[64:65], 0, v[164:165]
	s_waitcnt vmcnt(0)
	v_mul_hi_i32 v3, v1, s35
	v_mul_lo_u32 v2, v1, s35
	v_lshl_add_u64 v[2:3], s[16:17], 0, v[2:3]
	v_lshl_add_u64 v[2:3], v[2:3], 0, s[22:23]
	v_lshl_add_u64 v[8:9], v[2:3], 0, s[20:21]
	v_readfirstlane_b32 s22, v2
	v_readfirstlane_b32 s23, v3
	v_readfirstlane_b32 s24, v8
	v_readfirstlane_b32 s25, v9
	v_lshl_add_u64 v[14:15], v[2:3], 0, v[162:163]
	v_lshl_add_u64 v[12:13], v[2:3], 0, v[164:165]
	v_lshl_add_u64 v[6:7], v[8:9], 0, v[162:163]
	global_load_lds_dwordx4 v4, s[22:23]
	s_add_i32 m0, s44, 0x12000
	s_nop 0
	global_load_lds_dwordx4 v164, s[22:23]
	s_add_i32 m0, s44, 0x14000
	s_nop 0
	global_load_lds_dwordx4 v4, s[24:25]
	s_add_i32 m0, s44, 0x16000
	s_add_u32 s22, s64, s20
	global_load_lds_dwordx4 v164, s[24:25]
	s_mov_b32 m0, s44
	s_addc_u32 s23, s65, s21
	global_load_lds_dwordx4 v4, s[64:65]
	s_add_i32 s49, s44, 0x4000
	s_mov_b32 m0, s45
	s_add_i32 s50, s44, 0x6000
	global_load_lds_dwordx4 v164, s[64:65]
	s_mov_b32 m0, s49
	s_cmp_eq_u32 s28, 1
	global_load_lds_dwordx4 v4, s[22:23]
	s_mov_b32 m0, s50
	v_lshl_add_u64 v[4:5], v[8:9], 0, v[164:165]
	global_load_lds_dwordx4 v164, s[22:23]
	v_lshl_add_u64 v[8:9], s[64:65], 0, v[162:163]
	s_cselect_b64 s[22:23], -1, 0
	s_cmp_lg_u32 s28, 1
	s_cbranch_scc1 .LBB0_2252
	s_barrier

;     ...
;     for (;;) {
;         const bool has_next = S.next(ui + 1, nxt);
;         const char* nA = has_next ? nxt.A : cA; const char* nB = has_next ? nxt.B : cB;
;     __device__ __forceinline__ bool next(int i, pg8::Unit& u) const {
;         const int T = tiles[0]; const long Lx = (long)i * G + c; if (Lx >= (long)T * nN) return false;
;         pg8::tile_of((int)Lx, T, nN, u.pm, u.pn); const int e = tiles[1 + u.pm]; u.z = e;
;         u.A = A0 + (size_t)u.pm * tsA; u.B = B0 + (size_t)e * estride + (size_t)u.pn * tsB; return true;
;     }
.LBB0_2255:
	v_mov_b32_e32 v252, v254
	v_mov_b32_e32 v253, v255
	s_add_i32 s51, s51, 1
	s_mul_i32 s4, s51, s68
	s_mul_hi_u32 s5, s51, s33
	s_mul_i32 s39, s51, s33
	s_add_i32 s5, s5, s4
	s_add_u32 s66, s39, s2
	s_addc_u32 s67, s5, s3
	s_bfe_u64 s[38:39], s[100:101], 0x70031
	s_mov_b32 s39, s38
	v_mov_b32_e32 v4, s38
	v_mul_hi_i32 v5, v4, 56
	v_mul_lo_u32 v4, v4, 56
	v_cmp_ge_i64_e32 vcc, s[66:67], v[4:5]
	v_cmp_lt_i64_e64 s[4:5], s[66:67], v[4:5]
	s_cbranch_vccnz .LBB0_2257
	s_ashr_i32 s40, s66, 31
	s_lshr_b32 s40, s40, 29
	s_add_i32 s40, s66, s40
	s_ashr_i32 s41, s40, 3
	s_and_b32 s40, s40, -8
	s_sub_i32 s40, s66, s40
	s_mul_i32 s38, s39, 7
	s_lshr_b32 s46, s40, 31
	s_add_i32 s38, s38, s46
	s_mul_i32 s38, s40, s38
	s_add_i32 s38, s38, s41
	s_mul_hi_i32 s40, s38, 0x92492493
	s_add_i32 s40, s40, s38
	s_lshr_b32 s41, s40, 31
	s_ashr_i32 s40, s40, 8
	s_add_i32 s40, s40, s41
	s_lshl_b32 s41, s40, 3
	s_sub_i32 s39, s39, s41
	s_min_i32 s39, s39, 8
	s_abs_i32 s46, s39
	v_cvt_f32_u32_e32 v4, s46
	s_sub_i32 s66, 0, s46
	s_mulk_i32 s40, 0x1c0
	s_sub_i32 s40, s38, s40
	v_rcp_iflag_f32_e32 v4, v4
	s_abs_i32 s38, s40
	s_xor_b32 s47, s40, s39
	s_ashr_i32 s47, s47, 31
	v_mul_f32_e32 v4, 0x4f7ffffe, v4
	v_cvt_u32_f32_e32 v4, v4
	s_nop 0
	v_readfirstlane_b32 s67, v4
	s_mul_i32 s66, s66, s67
	s_mul_hi_u32 s66, s67, s66
	s_add_i32 s67, s67, s66
	s_mul_hi_u32 s66, s38, s67
	s_mul_i32 s67, s66, s46
	s_sub_i32 s38, s38, s67
	s_add_i32 s67, s66, 1
	s_sub_i32 s72, s38, s46
	s_cmp_ge_u32 s38, s46
	s_cselect_b32 s66, s67, s66
	s_cselect_b32 s38, s72, s38
	s_add_i32 s67, s66, 1
	s_cmp_ge_u32 s38, s46
	s_cselect_b32 s38, s67, s66
	s_xor_b32 s38, s38, s47
	s_sub_i32 s38, s38, s47
	s_mul_i32 s39, s38, s39
	s_sub_i32 s39, s40, s39
	s_add_i32 s40, s41, s39
	s_ashr_i32 s41, s40, 31
	s_lshl_b64 s[46:47], s[40:41], 2
	s_add_u32 s46, s10, s46
	s_addc_u32 s47, s11, s47
	s_mov_b32 s66, 0
	s_bfe_u64 s[46:47], s[100:101], 0x70000
	s_cmp_ge_u32 s40, s46
	s_addc_u32 s66, s66, 0
	s_bfe_u64 s[46:47], s[100:101], 0x70007
	s_cmp_ge_u32 s40, s46
	s_addc_u32 s66, s66, 0
	s_bfe_u64 s[46:47], s[100:101], 0x7000e
	s_cmp_ge_u32 s40, s46
	s_addc_u32 s66, s66, 0
	s_bfe_u64 s[46:47], s[100:101], 0x70015
	s_cmp_ge_u32 s40, s46
	s_addc_u32 s66, s66, 0
	s_bfe_u64 s[46:47], s[100:101], 0x7001c
	s_cmp_ge_u32 s40, s46
	s_addc_u32 s66, s66, 0
	s_bfe_u64 s[46:47], s[100:101], 0x70023
	s_cmp_ge_u32 s40, s46
	s_addc_u32 s66, s66, 0
	s_bfe_u64 s[46:47], s[100:101], 0x7002a
	s_cmp_ge_u32 s40, s46
	s_addc_u32 s66, s66, 0
	v_mov_b32_e32 v4, s66
	v_lshrrev_b32_e32 v254, 8, v0
	v_lshlrev_b32_e32 v254, 6, v254
	v_lshl_add_u32 v254, s40, 8, v254
	v_lshlrev_b32_e32 v254, 2, v254
	global_load_dword v255, v254, s[14:15] offset:512
	global_load_dword v254, v254, s[14:15]
	s_lshl_b64 s[46:47], s[40:41], 19
	s_add_u32 s46, s42, s46
	s_addc_u32 s47, s43, s47
	s_ashr_i32 s39, s38, 31
	s_lshl_b64 s[66:67], s[38:39], 19
	v_mul_hi_i32 v5, v4, s35
	v_mul_lo_u32 v4, v4, s35
	v_lshl_add_u64 v[4:5], s[16:17], 0, v[4:5]
	v_lshl_add_u64 v[172:173], v[4:5], 0, s[66:67]

; #define PG8_STAGE(bufoff, gbase, voff) do { _Pragma("unroll") for (int _i = 0; _i < 2; ++_i) \
;         __builtin_amdgcn_global_load_lds((const unsigned*)((const char*)(gbase) + (voff)[_i]), (LAS unsigned*)(lds + (bufoff) + ldsw + _i * 8192), 16, 0, 0); } while (0)
; #define PG8_LDA(dst, b, h) do { _Pragma("unroll") for (int m = 0; m < 4; ++m) dst[m] = PG8_LD8(lds + PG8_SA(b, h) + aoff + m * 2048); } while (0)
; #define PG8_LDB(dst, b, h) do { _Pragma("unroll") for (int n = 0; n < 2; ++n) dst[n] = PG8_LD8(lds + PG8_SB(b, h) + boff + n * 2048); } while (0)
; #define PG8_WAIT_V(n) asm volatile("s_waitcnt vmcnt(" #n ")" ::: "memory")
; #define PG8_WAIT_L(n) asm volatile("s_waitcnt lgkmcnt(" #n ")" ::: "memory")
; #define PG8_BAR __builtin_amdgcn_s_barrier()
; #define PG8_SCHED __builtin_amdgcn_sched_barrier(0)
;     ...
;         for (int t = 0; t < nt; t += 2) {
;             const bool last = (t == nt - 2);
;             const char* a1 = cA + (size_t)(t + 1) * kstep;
;             const char* a2 = last ? nA : cA + (size_t)(t + 2) * kstep; const char* b2 = last ? nB : cB + (size_t)(t + 2) * kstep;
;             const char* a3 = a2 + kstep; const char* b3 = b2 + kstep;
;             if constexpr (SP2) {
;             PG8_LDB(B0, 0, 0); PG8_LDB(B1, 0, 1); PG8_SCHED; PG8_LDA(At, 0, 0); PG8_STAGE(PG8_SA(1, 1), a1 + hstep, voffA);
;             PG8_WAIT_V(8); PG8_WAIT_L(0); PG8_BAR; PG8_MMA(0, 0, At, B0); PG8_MMA(0, 1, At, B1); PG8_BAR; PG8_SCHED;
;             PG8_LDA(At, 0, 1); PG8_STAGE(PG8_SB(0, 0), b2, voffB); PG8_STAGE(PG8_SB(0, 1), b2 + hstep, voffB); PG8_STAGE(PG8_SA(0, 0), a2, voffA);
;             PG8_WAIT_V(8); PG8_WAIT_L(0); PG8_BAR; PG8_MMA(1, 0, At, B0); PG8_MMA(1, 1, At, B1); PG8_BAR; PG8_SCHED;
.LBB0_2259:
	ds_read_b128 v[18:21], v166
	ds_read_b128 v[22:25], v166 offset:1024
	ds_read_b128 v[26:29], v166 offset:2048
	ds_read_b128 v[30:33], v166 offset:3072
	ds_read_b128 v[2:5], v190
	ds_read_b128 v[6:9], v190 offset:1024
	ds_read_b128 v[10:13], v190 offset:2048
	ds_read_b128 v[14:17], v190 offset:3072
	s_add_i32 s39, s41, 2
	s_add_u32 s66, s64, 0x80
	s_addc_u32 s67, s65, 0
	s_cmp_eq_u32 s63, s41
	s_cselect_b64 vcc, -1, 0
	s_cselect_b32 s67, s47, s67
	s_cselect_b32 s66, s46, s66
	v_cndmask_b32_e32 v185, v175, v173, vcc
	v_cndmask_b32_e32 v184, v174, v172, vcc
	v_lshl_add_u64 v[186:187], s[64:65], 0, v[168:169]
	s_add_i32 m0, s44, 0xc000
	ds_read_b128 v[176:179], v191
	ds_read_b128 v[180:183], v191 offset:1024
	ds_read_b128 v[196:199], v191 offset:2048
	ds_read_b128 v[200:203], v191 offset:3072
	ds_read_b128 v[204:207], v191 offset:4096
	ds_read_b128 v[208:211], v191 offset:5120
	ds_read_b128 v[212:215], v191 offset:6144
	ds_read_b128 v[216:219], v191 offset:7168
	global_load_lds_dwordx4 v[186:187], off
	v_lshl_add_u64 v[186:187], s[64:65], 0, v[170:171]
	s_add_i32 m0, s44, 0xe000
	s_nop 0
	global_load_lds_dwordx4 v[186:187], off
	s_waitcnt vmcnt(8)
	s_waitcnt lgkmcnt(0)
	s_barrier
	v_cmp_eq_f32_e32 vcc, 0, v252
	s_cbranch_vccnz .Lp21sk_0
	s_setprio 1
	s_waitcnt lgkmcnt(0)
	v_mfma_f32_16x16x128_f8f6f4 v[158:161], v[18:25], v[176:183], v[158:161]
	v_mfma_f32_16x16x128_f8f6f4 v[154:157], v[26:33], v[176:183], v[154:157]
	v_mfma_f32_16x16x128_f8f6f4 v[142:145], v[18:25], v[196:203], v[142:145]
	v_mfma_f32_16x16x128_f8f6f4 v[138:141], v[26:33], v[196:203], v[138:141]
	v_mfma_f32_16x16x128_f8f6f4 v[126:129], v[18:25], v[204:211], v[126:129]
	v_mfma_f32_16x16x128_f8f6f4 v[122:125], v[26:33], v[204:211], v[122:125]
	v_mfma_f32_16x16x128_f8f6f4 v[110:113], v[18:25], v[212:219], v[110:113]
	v_mfma_f32_16x16x128_f8f6f4 v[106:109], v[26:33], v[212:219], v[106:109]
	s_nop 7
	s_setprio 0
	s_setprio 1
	v_mfma_f32_16x16x128_f8f6f4 v[146:149], v[2:9], v[176:183], v[146:149]
	v_mfma_f32_16x16x128_f8f6f4 v[150:153], v[10:17], v[176:183], v[150:153]
	v_mfma_f32_16x16x128_f8f6f4 v[130:133], v[2:9], v[196:203], v[130:133]
	v_mfma_f32_16x16x128_f8f6f4 v[134:137], v[10:17], v[196:203], v[134:137]
	v_mfma_f32_16x16x128_f8f6f4 v[114:117], v[2:9], v[204:211], v[114:117]
	v_mfma_f32_16x16x128_f8f6f4 v[118:121], v[10:17], v[204:211], v[118:121]
	v_mfma_f32_16x16x128_f8f6f4 v[98:101], v[2:9], v[212:219], v[98:101]
	v_mfma_f32_16x16x128_f8f6f4 v[102:105], v[10:17], v[212:219], v[102:105]
	s_nop 7
	s_setprio 0
.Lp21sk_0:
	s_barrier
	s_add_i32 s41, s69, s34
	v_lshl_add_u64 v[176:177], v[184:185], 0, v[162:163]
	s_mov_b32 m0, s41
	ds_read_b128 v[196:199], v191 offset:16384
	ds_read_b128 v[200:203], v191 offset:17408
	ds_read_b128 v[204:207], v191 offset:18432
	ds_read_b128 v[208:211], v191 offset:19456
	ds_read_b128 v[212:215], v191 offset:20480
	ds_read_b128 v[216:219], v191 offset:21504
	ds_read_b128 v[220:223], v191 offset:22528
	ds_read_b128 v[224:227], v191 offset:23552
	global_load_lds_dwordx4 v[176:177], off
	v_lshl_add_u64 v[178:179], v[184:185], 0, v[164:165]
	s_add_i32 m0, s41, 0x2000
	v_lshl_add_u64 v[182:183], v[184:185], 0, s[20:21]
	s_add_i32 s41, s70, s34
	global_load_lds_dwordx4 v[178:179], off
	v_lshl_add_u64 v[180:181], v[182:183], 0, v[162:163]
	s_mov_b32 m0, s41
	v_lshl_add_u64 v[182:183], v[182:183], 0, v[164:165]
	global_load_lds_dwordx4 v[180:181], off
	s_add_i32 m0, s41, 0x2000
	v_lshl_add_u64 v[184:185], s[66:67], 0, v[162:163]
	global_load_lds_dwordx4 v[182:183], off
	s_mov_b32 m0, s44
	v_lshl_add_u64 v[186:187], s[66:67], 0, v[164:165]
	global_load_lds_dwordx4 v[184:185], off
	s_mov_b32 m0, s45
	s_nop 0
	global_load_lds_dwordx4 v[186:187], off
	s_waitcnt vmcnt(8)
	s_waitcnt lgkmcnt(0)
	s_barrier
	v_cmp_eq_f32_e32 vcc, 0, v253
	s_cbranch_vccnz .Lp21sk_1
	s_setprio 1
	s_waitcnt lgkmcnt(0)
	v_mfma_f32_16x16x128_f8f6f4 v[94:97], v[18:25], v[196:203], v[94:97]
	v_mfma_f32_16x16x128_f8f6f4 v[90:93], v[26:33], v[196:203], v[90:93]
	v_mfma_f32_16x16x128_f8f6f4 v[78:81], v[18:25], v[204:211], v[78:81]
	v_mfma_f32_16x16x128_f8f6f4 v[74:77], v[26:33], v[204:211], v[74:77]
	v_mfma_f32_16x16x128_f8f6f4 v[62:65], v[18:25], v[212:219], v[62:65]
	v_mfma_f32_16x16x128_f8f6f4 v[58:61], v[26:33], v[212:219], v[58:61]
	v_mfma_f32_16x16x128_f8f6f4 v[46:49], v[18:25], v[220:227], v[46:49]
	v_mfma_f32_16x16x128_f8f6f4 v[42:45], v[26:33], v[220:227], v[42:45]
	s_nop 7
	s_setprio 0
	s_setprio 1
	v_mfma_f32_16x16x128_f8f6f4 v[82:85], v[2:9], v[196:203], v[82:85]
	v_mfma_f32_16x16x128_f8f6f4 v[86:89], v[10:17], v[196:203], v[86:89]
	v_mfma_f32_16x16x128_f8f6f4 v[66:69], v[2:9], v[204:211], v[66:69]
	v_mfma_f32_16x16x128_f8f6f4 v[70:73], v[10:17], v[204:211], v[70:73]
	v_mfma_f32_16x16x128_f8f6f4 v[50:53], v[2:9], v[212:219], v[50:53]
	v_mfma_f32_16x16x128_f8f6f4 v[54:57], v[10:17], v[212:219], v[54:57]
	v_mfma_f32_16x16x128_f8f6f4 v[34:37], v[2:9], v[220:227], v[34:37]
	v_mfma_f32_16x16x128_f8f6f4 v[38:41], v[10:17], v[220:227], v[38:41]
	s_nop 7
	s_setprio 0
; #define PG8_STAGE(bufoff, gbase, voff) do { _Pragma("unroll") for (int _i = 0; _i < 2; ++_i) \
;         __builtin_amdgcn_global_load_lds((const unsigned*)((const char*)(gbase) + (voff)[_i]), (LAS unsigned*)(lds + (bufoff) + ldsw + _i * 8192), 16, 0, 0); } while (0)
; #define PG8_LDA(dst, b, h) do { _Pragma("unroll") for (int m = 0; m < 4; ++m) dst[m] = PG8_LD8(lds + PG8_SA(b, h) + aoff + m * 2048); } while (0)
; #define PG8_LDB(dst, b, h) do { _Pragma("unroll") for (int n = 0; n < 2; ++n) dst[n] = PG8_LD8(lds + PG8_SB(b, h) + boff + n * 2048); } while (0)
; #define PG8_WAIT_V(n) asm volatile("s_waitcnt vmcnt(" #n ")" ::: "memory")
; #define PG8_WAIT_L(n) asm volatile("s_waitcnt lgkmcnt(" #n ")" ::: "memory")
; #define PG8_BAR __builtin_amdgcn_s_barrier()
; #define PG8_SCHED __builtin_amdgcn_sched_barrier(0)
;     ...
;             PG8_LDB(B0, 1, 0); PG8_LDB(B1, 1, 1); PG8_SCHED; PG8_LDA(At, 1, 0); PG8_STAGE(PG8_SA(0, 1), a2 + hstep, voffA);
;             PG8_WAIT_V(8); PG8_WAIT_L(0); PG8_BAR; PG8_MMA(0, 0, At, B0); PG8_MMA(0, 1, At, B1); PG8_BAR; PG8_SCHED;
;             PG8_LDA(At, 1, 1); PG8_STAGE(PG8_SB(1, 0), b3, voffB); PG8_STAGE(PG8_SB(1, 1), b3 + hstep, voffB); PG8_STAGE(PG8_SA(1, 0), a3, voffA);
;             PG8_WAIT_V(8); PG8_WAIT_L(0); PG8_BAR; PG8_MMA(1, 0, At, B0); PG8_MMA(1, 1, At, B1); PG8_BAR; PG8_SCHED;
.Lp21sk_1:
	s_barrier
	s_add_i32 s41, 0, 0x18000
	s_add_i32 s72, 0, 0x1c000
	v_add_u32_e32 v14, s41, v188
	v_add_u32_e32 v30, s72, v188
	ds_read_b128 v[2:5], v14
	ds_read_b128 v[6:9], v14 offset:1024
	ds_read_b128 v[10:13], v14 offset:2048
	ds_read_b128 v[14:17], v14 offset:3072
	ds_read_b128 v[18:21], v30
	ds_read_b128 v[22:25], v30 offset:1024
	ds_read_b128 v[26:29], v30 offset:2048
	ds_read_b128 v[30:33], v30 offset:3072
	s_add_u32 s66, s66, s20
	s_addc_u32 s67, s67, s21
	s_mov_b32 m0, s49
	v_lshl_add_u64 v[192:193], s[66:67], 0, v[162:163]
	ds_read_b128 v[196:199], v191 offset:32768
	ds_read_b128 v[200:203], v191 offset:33792
	ds_read_b128 v[204:207], v191 offset:34816
	ds_read_b128 v[208:211], v191 offset:35840
	ds_read_b128 v[212:215], v191 offset:36864
	ds_read_b128 v[216:219], v191 offset:37888
	ds_read_b128 v[220:223], v191 offset:38912
	ds_read_b128 v[224:227], v191 offset:39936
	global_load_lds_dwordx4 v[192:193], off
	v_lshl_add_u64 v[192:193], s[66:67], 0, v[164:165]
	s_mov_b32 m0, s50
	s_nop 0
	global_load_lds_dwordx4 v[192:193], off
	s_waitcnt vmcnt(8)
	s_waitcnt lgkmcnt(0)
	s_barrier
	v_cmp_eq_f32_e32 vcc, 0, v252
	s_cbranch_vccnz .Lp21sk_2
	s_setprio 1
	s_waitcnt lgkmcnt(0)
	v_mfma_f32_16x16x128_f8f6f4 v[158:161], v[2:9], v[196:203], v[158:161]
	v_mfma_f32_16x16x128_f8f6f4 v[154:157], v[10:17], v[196:203], v[154:157]
	v_mfma_f32_16x16x128_f8f6f4 v[142:145], v[2:9], v[204:211], v[142:145]
	v_mfma_f32_16x16x128_f8f6f4 v[138:141], v[10:17], v[204:211], v[138:141]
	v_mfma_f32_16x16x128_f8f6f4 v[126:129], v[2:9], v[212:219], v[126:129]
	v_mfma_f32_16x16x128_f8f6f4 v[122:125], v[10:17], v[212:219], v[122:125]
	v_mfma_f32_16x16x128_f8f6f4 v[110:113], v[2:9], v[220:227], v[110:113]
	v_mfma_f32_16x16x128_f8f6f4 v[106:109], v[10:17], v[220:227], v[106:109]
	s_nop 7
	s_setprio 0
	s_setprio 1
	v_mfma_f32_16x16x128_f8f6f4 v[146:149], v[18:25], v[196:203], v[146:149]
	v_mfma_f32_16x16x128_f8f6f4 v[150:153], v[26:33], v[196:203], v[150:153]
	v_mfma_f32_16x16x128_f8f6f4 v[130:133], v[18:25], v[204:211], v[130:133]
	v_mfma_f32_16x16x128_f8f6f4 v[134:137], v[26:33], v[204:211], v[134:137]
	v_mfma_f32_16x16x128_f8f6f4 v[114:117], v[18:25], v[212:219], v[114:117]
	v_mfma_f32_16x16x128_f8f6f4 v[118:121], v[26:33], v[212:219], v[118:121]
	v_mfma_f32_16x16x128_f8f6f4 v[98:101], v[18:25], v[220:227], v[98:101]
	v_mfma_f32_16x16x128_f8f6f4 v[102:105], v[26:33], v[220:227], v[102:105]
	s_nop 7
	s_setprio 0
.Lp21sk_2:
	s_barrier
	s_add_i32 s41, s41, s34
	v_lshl_add_u64 v[176:177], v[176:177], 0, s[24:25]
	s_mov_b32 m0, s41
	ds_read_b128 v[196:199], v191 offset:49152
	ds_read_b128 v[200:203], v191 offset:50176
	ds_read_b128 v[204:207], v191 offset:51200
	ds_read_b128 v[208:211], v191 offset:52224
	ds_read_b128 v[212:215], v191 offset:53248
	ds_read_b128 v[216:219], v191 offset:54272
	ds_read_b128 v[220:223], v191 offset:55296
	ds_read_b128 v[224:227], v191 offset:56320
	global_load_lds_dwordx4 v[176:177], off
	v_lshl_add_u64 v[176:177], v[178:179], 0, s[24:25]
	s_add_i32 m0, s41, 0x2000
	s_add_i32 s41, s72, s34
	global_load_lds_dwordx4 v[176:177], off
	v_lshl_add_u64 v[176:177], v[180:181], 0, s[24:25]
	s_mov_b32 m0, s41
	s_nop 0
	global_load_lds_dwordx4 v[176:177], off
	v_lshl_add_u64 v[176:177], v[182:183], 0, s[24:25]
	s_add_i32 m0, s41, 0x2000
	s_nop 0
	global_load_lds_dwordx4 v[176:177], off
	v_lshl_add_u64 v[176:177], v[184:185], 0, s[24:25]
	s_mov_b32 m0, s56
	s_nop 0
	global_load_lds_dwordx4 v[176:177], off
	v_lshl_add_u64 v[176:177], v[186:187], 0, s[24:25]
	s_mov_b32 m0, s57
	s_nop 0
	global_load_lds_dwordx4 v[176:177], off
	s_waitcnt vmcnt(8)
	s_waitcnt lgkmcnt(0)
	s_barrier
	v_cmp_eq_f32_e32 vcc, 0, v253
	s_cbranch_vccnz .Lp21sk_3
	s_setprio 1
	s_waitcnt lgkmcnt(0)
	v_mfma_f32_16x16x128_f8f6f4 v[94:97], v[2:9], v[196:203], v[94:97]
	v_mfma_f32_16x16x128_f8f6f4 v[90:93], v[10:17], v[196:203], v[90:93]
	v_mfma_f32_16x16x128_f8f6f4 v[78:81], v[2:9], v[204:211], v[78:81]
	v_mfma_f32_16x16x128_f8f6f4 v[74:77], v[10:17], v[204:211], v[74:77]
	v_mfma_f32_16x16x128_f8f6f4 v[62:65], v[2:9], v[212:219], v[62:65]
	v_mfma_f32_16x16x128_f8f6f4 v[58:61], v[10:17], v[212:219], v[58:61]
	v_mfma_f32_16x16x128_f8f6f4 v[46:49], v[2:9], v[220:227], v[46:49]
	v_mfma_f32_16x16x128_f8f6f4 v[42:45], v[10:17], v[220:227], v[42:45]
	s_nop 7
	s_setprio 0
	s_setprio 1
	v_mfma_f32_16x16x128_f8f6f4 v[82:85], v[18:25], v[196:203], v[82:85]
	v_mfma_f32_16x16x128_f8f6f4 v[86:89], v[26:33], v[196:203], v[86:89]
	v_mfma_f32_16x16x128_f8f6f4 v[66:69], v[18:25], v[204:211], v[66:69]
	v_mfma_f32_16x16x128_f8f6f4 v[70:73], v[26:33], v[204:211], v[70:73]
	v_mfma_f32_16x16x128_f8f6f4 v[50:53], v[18:25], v[212:219], v[50:53]
	v_mfma_f32_16x16x128_f8f6f4 v[54:57], v[26:33], v[212:219], v[54:57]
	v_mfma_f32_16x16x128_f8f6f4 v[34:37], v[18:25], v[220:227], v[34:37]
	v_mfma_f32_16x16x128_f8f6f4 v[38:41], v[26:33], v[220:227], v[38:41]
	s_nop 7
	s_setprio 0
.Lp21sk_3:
	s_barrier
	s_add_u32 s64, s64, 0x100
	s_addc_u32 s65, s65, 0
	v_lshl_add_u64 v[174:175], v[174:175], 0, s[36:37]
	s_cmp_ge_i32 s39, s59
	s_mov_b32 s41, s39
	s_cbranch_scc0 .LBB0_2259

; __device__ __forceinline__ float sigm(float x) { return __builtin_amdgcn_rcpf(1.f + __builtin_amdgcn_exp2f(-1.4426950408889634f * x)); }
; __device__ __forceinline__ unsigned pk4_fp8(float a, float b, float c, float d) { int w = 0; w = __builtin_amdgcn_cvt_pk_fp8_f32(a, b, w, false); w = __builtin_amdgcn_cvt_pk_fp8_f32(c, d, w, true); return (unsigned)w; }
; __device__ __forceinline__ u32x4 pack8(f32x4 v0, f32x4 v1) { u32x4 w; w.x = cvt_pk_bf16(v0[0], v0[1]); w.y = cvt_pk_bf16(v0[2], v0[3]); w.z = cvt_pk_bf16(v1[0], v1[1]); w.w = cvt_pk_bf16(v1[2], v1[3]); return w; }
; template <class T> __device__ __forceinline__ void est(T* p, T v) { if constexpr (MK_EPI_NT != 0) __builtin_nontemporal_store(v, p); else *p = v; }
; __device__ __forceinline__ float ss_val(const ss_t* ss, int row) { return (float)ss[row] * (1.f / 16777216.f); }
;     __device__ __forceinline__ void operator()(AccT acc, const Unit& u, int wr, int wc, int fr, int fq) const {
;         const int row0 = u.pm * 256 + wr * 64 + fr, col0 = u.pn * 128 + wc * 32 + 8 * fq;
; #pragma unroll
;         for (int ai = 0; ai < 2; ++ai)
; #pragma unroll
;             for (int m = 0; m < 4; ++m) { const int row = row0 + ai * 128 + m * 16; const float r = (is_rstd ? ((const float*)rs)[row] : rsqrtf(ss_val((const ss_t*)rs, row) * (1.0f / DM) + EPS)) * ascale;
;                 f32x4 o[2];
; #pragma unroll
;                 for (int bj = 0; bj < 2; ++bj) { const f32x4 a = acc[ai][bj][m][0] * r, b = acc[ai][bj][m][1] * r;
; #pragma unroll
;                     for (int j = 0; j < 4; ++j) o[bj][j] = a[j] * sigm(a[j]) * b[j]; }
;                 if constexpr (F8OUT) est((u32x2*)((unsigned char*)O + (size_t)row * ldo + col0), (u32x2)(u32x2){pk4_fp8(o[0][0], o[0][1], o[0][2], o[0][3]), pk4_fp8(o[1][0], o[1][1], o[1][2], o[1][3])});
;                 else est((u32x4*)((bf16_t*)O + (size_t)row * ldo + col0), (u32x4)pack8(o[0], o[1])); }
.LBB0_2262:
	v_lshl_add_u32 v2, s62, 8, v1
	v_ashrrev_i32_e32 v3, 31, v2
	s_nop 15
	s_nop 15
	v_lshl_add_u64 v[8:9], v[2:3], 2, s[14:15]
	global_load_dword v248, v[8:9], off
	global_load_dword v249, v[8:9], off offset:64
	global_load_dword v250, v[8:9], off offset:128
	global_load_dword v251, v[8:9], off offset:192
	v_mov_b32_e32 v4, v154
	v_mov_b32_e32 v6, v150
	v_mov_b32_e32 v20, v151
	v_mov_b32_e32 v24, v152
	v_mov_b32_e32 v28, 0
	v_mov_b32_e32 v29, 0
	v_mov_b32_e32 v26, v153
	v_or_b32_e32 v32, 16, v2
	v_ashrrev_i32_e32 v33, 31, v32
	s_andn2_b64 vcc, exec, s[4:5]
	s_mov_b64 s[4:5], -1
	s_waitcnt vmcnt(3)
	v_mov_b32_e32 v3, v248
	global_load_dword v248, v[8:9], off offset:512
	v_mul_f32_e32 v10, 0x3d000000, v3
	v_mul_f32_e32 v11, v158, v10
	v_mul_f32_e32 v3, 0xbfb8aa3b, v11
	v_exp_f32_e32 v3, v3
	s_nop 0
	v_add_f32_e32 v3, 1.0, v3
	v_rcp_f32_e32 v5, v3
	s_nop 0
	v_pk_mul_f32 v[12:13], v[4:5], v[10:11]
	v_mul_f32_e32 v11, v159, v10
	v_mul_f32_e32 v3, 0xbfb8aa3b, v11
	v_exp_f32_e32 v3, v3
	v_mov_b32_e32 v4, v155
	v_mul_f32_e32 v12, v12, v13
	v_add_f32_e32 v3, 1.0, v3
	v_rcp_f32_e32 v5, v3
	s_nop 0
	v_pk_mul_f32 v[14:15], v[4:5], v[10:11]
	v_mul_f32_e32 v11, v160, v10
	v_mul_f32_e32 v3, 0xbfb8aa3b, v11
	v_exp_f32_e32 v3, v3
	v_mov_b32_e32 v4, v156
	v_add_f32_e32 v3, 1.0, v3
	v_rcp_f32_e32 v5, v3
	s_nop 0
	v_pk_mul_f32 v[16:17], v[4:5], v[10:11]
	v_mul_f32_e32 v11, v161, v10
	v_mul_f32_e32 v3, 0xbfb8aa3b, v11
	v_exp_f32_e32 v3, v3
	v_mov_b32_e32 v4, v157
	v_add_f32_e32 v3, 1.0, v3
	v_rcp_f32_e32 v5, v3
	s_nop 0
	v_pk_mul_f32 v[18:19], v[4:5], v[10:11]
	v_mul_f32_e32 v11, v146, v10
	v_mul_f32_e32 v3, 0xbfb8aa3b, v11
	v_exp_f32_e32 v3, v3
	v_lshl_or_b32 v4, s48, 7, v189
	v_ashrrev_i32_e32 v5, 31, v4
	v_add_f32_e32 v3, 1.0, v3
	v_rcp_f32_e32 v7, v3
	s_nop 0
	v_pk_mul_f32 v[22:23], v[6:7], v[10:11]
	v_mul_f32_e32 v11, v147, v10
	v_mul_f32_e32 v3, 0xbfb8aa3b, v11
	v_exp_f32_e32 v3, v3
	v_mov_b64_e32 v[6:7], s[12:13]
	v_mad_i64_i32 v[30:31], s[64:65], v2, s71, v[6:7]
	v_add_f32_e32 v3, 1.0, v3
	v_rcp_f32_e32 v21, v3
	s_nop 0
	v_pk_mul_f32 v[20:21], v[20:21], v[10:11]
	v_mul_f32_e32 v11, v148, v10
	v_mul_f32_e32 v3, 0xbfb8aa3b, v11
	v_exp_f32_e32 v3, v3
	s_nop 0
	v_add_f32_e32 v3, 1.0, v3
	v_rcp_f32_e32 v25, v3
	v_mul_f32_e32 v3, v14, v15
	v_cvt_pk_fp8_f32 v28, v12, v3
	v_mul_f32_e32 v3, v16, v17
	v_pk_mul_f32 v[12:13], v[24:25], v[10:11]
	v_mul_f32_e32 v11, v149, v10
	v_mul_f32_e32 v14, 0xbfb8aa3b, v11
	v_exp_f32_e32 v14, v14
	v_mul_f32_e32 v15, v18, v19
	v_cvt_pk_fp8_f32 v28, v3, v15 op_sel:[0,0,1]
	v_mul_f32_e32 v3, v22, v23
	v_add_f32_e32 v14, 1.0, v14
	v_rcp_f32_e32 v27, v14
	v_mul_f32_e32 v14, v20, v21
	v_cvt_pk_fp8_f32 v29, v3, v14
	v_mul_f32_e32 v3, v12, v13
	v_pk_mul_f32 v[10:11], v[26:27], v[10:11]
	v_lshl_add_u64 v[12:13], v[32:33], 2, s[14:15]
	v_mul_f32_e32 v10, v10, v11
	v_cvt_pk_fp8_f32 v29, v3, v10 op_sel:[0,0,1]
	v_lshl_add_u64 v[10:11], v[30:31], 0, v[4:5]
	v_mov_b32_e32 v14, v139
	v_mov_b32_e32 v16, v140
	global_store_dwordx2 v[10:11], v[28:29], off
	s_nop 0
	v_mov_b32_e32 v12, v138
	v_mov_b32_e32 v18, v141
	v_mov_b32_e32 v20, v134
	v_mov_b32_e32 v22, v135
	v_mov_b32_e32 v24, v136
	v_mov_b32_e32 v28, 0
	v_mov_b32_e32 v29, 0
	v_mov_b32_e32 v26, v137
	v_or_b32_e32 v30, 32, v2
	v_mad_i64_i32 v[32:33], s[64:65], v32, s71, v[6:7]
	v_ashrrev_i32_e32 v31, 31, v30
	s_waitcnt vmcnt(4)
	v_mov_b32_e32 v3, v249
	global_load_dword v249, v[8:9], off offset:576
	v_mul_f32_e32 v10, 0x3d000000, v3
	v_mul_f32_e32 v11, v142, v10
	v_mul_f32_e32 v3, 0xbfb8aa3b, v11
	v_exp_f32_e32 v3, v3
	s_nop 0
	v_add_f32_e32 v3, 1.0, v3
	v_rcp_f32_e32 v13, v3
	s_nop 0
	v_pk_mul_f32 v[12:13], v[12:13], v[10:11]
	v_mul_f32_e32 v11, v143, v10
	v_mul_f32_e32 v3, 0xbfb8aa3b, v11
	v_exp_f32_e32 v3, v3
	v_mul_f32_e32 v12, v12, v13
	v_add_f32_e32 v3, 1.0, v3
	v_rcp_f32_e32 v15, v3
	s_nop 0
	v_pk_mul_f32 v[14:15], v[14:15], v[10:11]
	v_mul_f32_e32 v11, v144, v10
	v_mul_f32_e32 v3, 0xbfb8aa3b, v11
	v_exp_f32_e32 v3, v3
	s_nop 0
	v_add_f32_e32 v3, 1.0, v3
	v_rcp_f32_e32 v17, v3
	s_nop 0
	v_pk_mul_f32 v[16:17], v[16:17], v[10:11]
	v_mul_f32_e32 v11, v145, v10
	v_mul_f32_e32 v3, 0xbfb8aa3b, v11
	v_exp_f32_e32 v3, v3
	s_nop 0
	v_add_f32_e32 v3, 1.0, v3
	v_rcp_f32_e32 v19, v3
	s_nop 0
	v_pk_mul_f32 v[18:19], v[18:19], v[10:11]
	v_mul_f32_e32 v11, v130, v10
	v_mul_f32_e32 v3, 0xbfb8aa3b, v11
	v_exp_f32_e32 v3, v3
	s_nop 0
	v_add_f32_e32 v3, 1.0, v3
	v_rcp_f32_e32 v21, v3
	s_nop 0
	v_pk_mul_f32 v[20:21], v[20:21], v[10:11]
	v_mul_f32_e32 v11, v131, v10
	v_mul_f32_e32 v3, 0xbfb8aa3b, v11
	v_exp_f32_e32 v3, v3
	s_nop 0
	v_add_f32_e32 v3, 1.0, v3
	v_rcp_f32_e32 v23, v3
	s_nop 0
	v_pk_mul_f32 v[22:23], v[22:23], v[10:11]
	v_mul_f32_e32 v11, v132, v10
	v_mul_f32_e32 v3, 0xbfb8aa3b, v11
	v_exp_f32_e32 v3, v3
	s_nop 0
	v_add_f32_e32 v3, 1.0, v3
	v_rcp_f32_e32 v25, v3
	v_mul_f32_e32 v3, v14, v15
	v_cvt_pk_fp8_f32 v28, v12, v3
	v_mul_f32_e32 v3, v16, v17
	v_pk_mul_f32 v[12:13], v[24:25], v[10:11]
	v_mul_f32_e32 v11, v133, v10
	v_mul_f32_e32 v14, 0xbfb8aa3b, v11
	v_exp_f32_e32 v14, v14
	v_mul_f32_e32 v15, v18, v19
	v_cvt_pk_fp8_f32 v28, v3, v15 op_sel:[0,0,1]
	v_mul_f32_e32 v3, v20, v21
	v_add_f32_e32 v14, 1.0, v14
	v_rcp_f32_e32 v27, v14
	v_mul_f32_e32 v14, v22, v23
	v_cvt_pk_fp8_f32 v29, v3, v14
	v_mul_f32_e32 v3, v12, v13
	v_pk_mul_f32 v[10:11], v[26:27], v[10:11]
	v_lshl_add_u64 v[12:13], v[30:31], 2, s[14:15]
	v_mul_f32_e32 v10, v10, v11
	v_cvt_pk_fp8_f32 v29, v3, v10 op_sel:[0,0,1]
	v_lshl_add_u64 v[10:11], v[32:33], 0, v[4:5]
	v_mov_b32_e32 v14, v123
	v_mov_b32_e32 v16, v124
	global_store_dwordx2 v[10:11], v[28:29], off
	s_nop 0
	v_mov_b32_e32 v12, v122
	v_mov_b32_e32 v18, v125
	v_mov_b32_e32 v20, v118
	v_mov_b32_e32 v22, v119
	v_mov_b32_e32 v24, v120
	v_mov_b32_e32 v28, 0
	v_mov_b32_e32 v29, 0
	v_mov_b32_e32 v26, v121
	v_or_b32_e32 v32, 48, v2
	v_mad_i64_i32 v[30:31], s[64:65], v30, s71, v[6:7]
	v_ashrrev_i32_e32 v33, 31, v32
	s_waitcnt vmcnt(5)
; __device__ __forceinline__ float sigm(float x) { return __builtin_amdgcn_rcpf(1.f + __builtin_amdgcn_exp2f(-1.4426950408889634f * x)); }
; __device__ __forceinline__ unsigned pk4_fp8(float a, float b, float c, float d) { int w = 0; w = __builtin_amdgcn_cvt_pk_fp8_f32(a, b, w, false); w = __builtin_amdgcn_cvt_pk_fp8_f32(c, d, w, true); return (unsigned)w; }
; __device__ __forceinline__ u32x4 pack8(f32x4 v0, f32x4 v1) { u32x4 w; w.x = cvt_pk_bf16(v0[0], v0[1]); w.y = cvt_pk_bf16(v0[2], v0[3]); w.z = cvt_pk_bf16(v1[0], v1[1]); w.w = cvt_pk_bf16(v1[2], v1[3]); return w; }
; template <class T> __device__ __forceinline__ void est(T* p, T v) { if constexpr (MK_EPI_NT != 0) __builtin_nontemporal_store(v, p); else *p = v; }
; __device__ __forceinline__ float ss_val(const ss_t* ss, int row) { return (float)ss[row] * (1.f / 16777216.f); }
;     __device__ __forceinline__ void operator()(AccT acc, const Unit& u, int wr, int wc, int fr, int fq) const {
;         const int row0 = u.pm * 256 + wr * 64 + fr, col0 = u.pn * 128 + wc * 32 + 8 * fq;
; #pragma unroll
;         for (int ai = 0; ai < 2; ++ai)
; #pragma unroll
;             for (int m = 0; m < 4; ++m) { const int row = row0 + ai * 128 + m * 16; const float r = (is_rstd ? ((const float*)rs)[row] : rsqrtf(ss_val((const ss_t*)rs, row) * (1.0f / DM) + EPS)) * ascale;
;                 f32x4 o[2];
; #pragma unroll
;                 for (int bj = 0; bj < 2; ++bj) { const f32x4 a = acc[ai][bj][m][0] * r, b = acc[ai][bj][m][1] * r;
; #pragma unroll
;                     for (int j = 0; j < 4; ++j) o[bj][j] = a[j] * sigm(a[j]) * b[j]; }
;                 if constexpr (F8OUT) est((u32x2*)((unsigned char*)O + (size_t)row * ldo + col0), (u32x2)(u32x2){pk4_fp8(o[0][0], o[0][1], o[0][2], o[0][3]), pk4_fp8(o[1][0], o[1][1], o[1][2], o[1][3])});
;                 else est((u32x4*)((bf16_t*)O + (size_t)row * ldo + col0), (u32x4)pack8(o[0], o[1])); }
	v_mov_b32_e32 v3, v250
	global_load_dword v250, v[8:9], off offset:640
	v_mul_f32_e32 v10, 0x3d000000, v3
	v_mul_f32_e32 v11, v126, v10
	v_mul_f32_e32 v3, 0xbfb8aa3b, v11
	v_exp_f32_e32 v3, v3
	s_nop 0
	v_add_f32_e32 v3, 1.0, v3
	v_rcp_f32_e32 v13, v3
	s_nop 0
	v_pk_mul_f32 v[12:13], v[12:13], v[10:11]
	v_mul_f32_e32 v11, v127, v10
	v_mul_f32_e32 v3, 0xbfb8aa3b, v11
	v_exp_f32_e32 v3, v3
	v_mul_f32_e32 v12, v12, v13
	v_add_f32_e32 v3, 1.0, v3
	v_rcp_f32_e32 v15, v3
	s_nop 0
	v_pk_mul_f32 v[14:15], v[14:15], v[10:11]
	v_mul_f32_e32 v11, v128, v10
	v_mul_f32_e32 v3, 0xbfb8aa3b, v11
	v_exp_f32_e32 v3, v3
	s_nop 0
	v_add_f32_e32 v3, 1.0, v3
	v_rcp_f32_e32 v17, v3
	s_nop 0
	v_pk_mul_f32 v[16:17], v[16:17], v[10:11]
	v_mul_f32_e32 v11, v129, v10
	v_mul_f32_e32 v3, 0xbfb8aa3b, v11
	v_exp_f32_e32 v3, v3
	s_nop 0
	v_add_f32_e32 v3, 1.0, v3
	v_rcp_f32_e32 v19, v3
	s_nop 0
	v_pk_mul_f32 v[18:19], v[18:19], v[10:11]
	v_mul_f32_e32 v11, v114, v10
	v_mul_f32_e32 v3, 0xbfb8aa3b, v11
	v_exp_f32_e32 v3, v3
	s_nop 0
	v_add_f32_e32 v3, 1.0, v3
	v_rcp_f32_e32 v21, v3
	s_nop 0
	v_pk_mul_f32 v[20:21], v[20:21], v[10:11]
	v_mul_f32_e32 v11, v115, v10
	v_mul_f32_e32 v3, 0xbfb8aa3b, v11
	v_exp_f32_e32 v3, v3
	s_nop 0
	v_add_f32_e32 v3, 1.0, v3
	v_rcp_f32_e32 v23, v3
	s_nop 0
	v_pk_mul_f32 v[22:23], v[22:23], v[10:11]
	v_mul_f32_e32 v11, v116, v10
	v_mul_f32_e32 v3, 0xbfb8aa3b, v11
	v_exp_f32_e32 v3, v3
	s_nop 0
	v_add_f32_e32 v3, 1.0, v3
	v_rcp_f32_e32 v25, v3
	v_mul_f32_e32 v3, v14, v15
	v_cvt_pk_fp8_f32 v28, v12, v3
	v_mul_f32_e32 v3, v16, v17
	v_pk_mul_f32 v[12:13], v[24:25], v[10:11]
	v_mul_f32_e32 v11, v117, v10
	v_mul_f32_e32 v14, 0xbfb8aa3b, v11
	v_exp_f32_e32 v14, v14
	v_mul_f32_e32 v15, v18, v19
	v_cvt_pk_fp8_f32 v28, v3, v15 op_sel:[0,0,1]
	v_mul_f32_e32 v3, v20, v21
	v_add_f32_e32 v14, 1.0, v14
	v_rcp_f32_e32 v27, v14
	v_mul_f32_e32 v14, v22, v23
	v_cvt_pk_fp8_f32 v29, v3, v14
	v_mul_f32_e32 v3, v12, v13
	v_pk_mul_f32 v[10:11], v[26:27], v[10:11]
	v_lshl_add_u64 v[12:13], v[32:33], 2, s[14:15]
	v_mul_f32_e32 v10, v10, v11
	v_cvt_pk_fp8_f32 v29, v3, v10 op_sel:[0,0,1]
	v_lshl_add_u64 v[10:11], v[30:31], 0, v[4:5]
	v_mov_b32_e32 v14, v107
	v_mov_b32_e32 v16, v108
	global_store_dwordx2 v[10:11], v[28:29], off
	s_nop 0
	v_mov_b32_e32 v12, v106
	v_mov_b32_e32 v18, v109
	v_mov_b32_e32 v20, v102
	v_mov_b32_e32 v22, v103
	v_mov_b32_e32 v24, v104
	v_mov_b32_e32 v28, 0
	v_mov_b32_e32 v29, 0
	v_mov_b32_e32 v26, v105
	v_add_u32_e32 v30, 0x80, v2
	s_waitcnt vmcnt(6)
	v_mov_b32_e32 v3, v251
	global_load_dword v251, v[8:9], off offset:704
	v_mul_f32_e32 v10, 0x3d000000, v3
	v_mul_f32_e32 v11, v110, v10
	v_mul_f32_e32 v3, 0xbfb8aa3b, v11
	v_exp_f32_e32 v3, v3
	s_nop 0
	v_add_f32_e32 v3, 1.0, v3
	v_rcp_f32_e32 v13, v3
	s_nop 0
	v_pk_mul_f32 v[12:13], v[12:13], v[10:11]
	v_mul_f32_e32 v11, v111, v10
	v_mul_f32_e32 v3, 0xbfb8aa3b, v11
	v_exp_f32_e32 v3, v3
	v_mul_f32_e32 v12, v12, v13
	v_add_f32_e32 v3, 1.0, v3
	v_rcp_f32_e32 v15, v3
	s_nop 0
	v_pk_mul_f32 v[14:15], v[14:15], v[10:11]
	v_mul_f32_e32 v11, v112, v10
	v_mul_f32_e32 v3, 0xbfb8aa3b, v11
	v_exp_f32_e32 v3, v3
	s_nop 0
	v_add_f32_e32 v3, 1.0, v3
	v_rcp_f32_e32 v17, v3
	s_nop 0
	v_pk_mul_f32 v[16:17], v[16:17], v[10:11]
	v_mul_f32_e32 v11, v113, v10
	v_mul_f32_e32 v3, 0xbfb8aa3b, v11
	v_exp_f32_e32 v3, v3
	s_nop 0
	v_add_f32_e32 v3, 1.0, v3
	v_rcp_f32_e32 v19, v3
	s_nop 0
	v_pk_mul_f32 v[18:19], v[18:19], v[10:11]
	v_mul_f32_e32 v11, v98, v10
	v_mul_f32_e32 v3, 0xbfb8aa3b, v11
	v_exp_f32_e32 v3, v3
	s_nop 0
	v_add_f32_e32 v3, 1.0, v3
	v_rcp_f32_e32 v21, v3
	s_nop 0
	v_pk_mul_f32 v[20:21], v[20:21], v[10:11]
	v_mul_f32_e32 v11, v99, v10
	v_mul_f32_e32 v3, 0xbfb8aa3b, v11
	v_exp_f32_e32 v3, v3
	s_nop 0
	v_add_f32_e32 v3, 1.0, v3
	v_rcp_f32_e32 v23, v3
	s_nop 0
	v_pk_mul_f32 v[22:23], v[22:23], v[10:11]
	v_mul_f32_e32 v11, v100, v10
	v_mul_f32_e32 v3, 0xbfb8aa3b, v11
	v_exp_f32_e32 v3, v3
	s_nop 0
	v_add_f32_e32 v3, 1.0, v3
	v_rcp_f32_e32 v25, v3
	v_mul_f32_e32 v3, v14, v15
	v_cvt_pk_fp8_f32 v28, v12, v3
	v_mul_f32_e32 v3, v16, v17
	v_pk_mul_f32 v[12:13], v[24:25], v[10:11]
	v_mul_f32_e32 v11, v101, v10
	v_mul_f32_e32 v14, 0xbfb8aa3b, v11
	v_exp_f32_e32 v14, v14
	v_mul_f32_e32 v15, v18, v19
	v_cvt_pk_fp8_f32 v28, v3, v15 op_sel:[0,0,1]
	v_mul_f32_e32 v3, v20, v21
	v_add_f32_e32 v14, 1.0, v14
	v_rcp_f32_e32 v27, v14
	v_mul_f32_e32 v14, v22, v23
	v_cvt_pk_fp8_f32 v29, v3, v14
	v_mul_f32_e32 v3, v12, v13
	v_pk_mul_f32 v[10:11], v[26:27], v[10:11]
	v_mov_b32_e32 v12, v90
	v_mul_f32_e32 v10, v10, v11
	v_cvt_pk_fp8_f32 v29, v3, v10 op_sel:[0,0,1]
	v_mad_i64_i32 v[10:11], s[64:65], v32, s71, v[6:7]
	v_lshl_add_u64 v[10:11], v[10:11], 0, v[4:5]
	global_store_dwordx2 v[10:11], v[28:29], off
	s_nop 0
	v_mov_b32_e32 v14, v91
	v_mov_b32_e32 v16, v92
	v_mov_b32_e32 v18, v93
	v_mov_b32_e32 v20, v86
	v_mov_b32_e32 v22, v87
	v_mov_b32_e32 v24, v88
	v_mov_b32_e32 v28, 0
	v_mov_b32_e32 v29, 0
	v_mov_b32_e32 v26, v89
	s_waitcnt vmcnt(7)
; __device__ __forceinline__ float sigm(float x) { return __builtin_amdgcn_rcpf(1.f + __builtin_amdgcn_exp2f(-1.4426950408889634f * x)); }
; __device__ __forceinline__ unsigned pk4_fp8(float a, float b, float c, float d) { int w = 0; w = __builtin_amdgcn_cvt_pk_fp8_f32(a, b, w, false); w = __builtin_amdgcn_cvt_pk_fp8_f32(c, d, w, true); return (unsigned)w; }
; __device__ __forceinline__ u32x4 pack8(f32x4 v0, f32x4 v1) { u32x4 w; w.x = cvt_pk_bf16(v0[0], v0[1]); w.y = cvt_pk_bf16(v0[2], v0[3]); w.z = cvt_pk_bf16(v1[0], v1[1]); w.w = cvt_pk_bf16(v1[2], v1[3]); return w; }
; template <class T> __device__ __forceinline__ void est(T* p, T v) { if constexpr (MK_EPI_NT != 0) __builtin_nontemporal_store(v, p); else *p = v; }
; __device__ __forceinline__ float ss_val(const ss_t* ss, int row) { return (float)ss[row] * (1.f / 16777216.f); }
;     __device__ __forceinline__ void operator()(AccT acc, const Unit& u, int wr, int wc, int fr, int fq) const {
;         const int row0 = u.pm * 256 + wr * 64 + fr, col0 = u.pn * 128 + wc * 32 + 8 * fq;
; #pragma unroll
;         for (int ai = 0; ai < 2; ++ai)
; #pragma unroll
;             for (int m = 0; m < 4; ++m) { const int row = row0 + ai * 128 + m * 16; const float r = (is_rstd ? ((const float*)rs)[row] : rsqrtf(ss_val((const ss_t*)rs, row) * (1.0f / DM) + EPS)) * ascale;
;                 f32x4 o[2];
; #pragma unroll
;                 for (int bj = 0; bj < 2; ++bj) { const f32x4 a = acc[ai][bj][m][0] * r, b = acc[ai][bj][m][1] * r;
; #pragma unroll
;                     for (int j = 0; j < 4; ++j) o[bj][j] = a[j] * sigm(a[j]) * b[j]; }
;                 if constexpr (F8OUT) est((u32x2*)((unsigned char*)O + (size_t)row * ldo + col0), (u32x2)(u32x2){pk4_fp8(o[0][0], o[0][1], o[0][2], o[0][3]), pk4_fp8(o[1][0], o[1][1], o[1][2], o[1][3])});
;                 else est((u32x4*)((bf16_t*)O + (size_t)row * ldo + col0), (u32x4)pack8(o[0], o[1])); }
	v_mov_b32_e32 v3, v248
	v_mul_f32_e32 v10, 0x3d000000, v3
	v_mul_f32_e32 v11, v94, v10
	v_mul_f32_e32 v3, 0xbfb8aa3b, v11
	v_exp_f32_e32 v3, v3
	s_nop 0
	v_add_f32_e32 v3, 1.0, v3
	v_rcp_f32_e32 v13, v3
	s_nop 0
	v_pk_mul_f32 v[12:13], v[12:13], v[10:11]
	v_mul_f32_e32 v11, v95, v10
	v_mul_f32_e32 v3, 0xbfb8aa3b, v11
	v_exp_f32_e32 v3, v3
	v_mul_f32_e32 v12, v12, v13
	v_add_f32_e32 v3, 1.0, v3
	v_rcp_f32_e32 v15, v3
	s_nop 0
	v_pk_mul_f32 v[14:15], v[14:15], v[10:11]
	v_mul_f32_e32 v11, v96, v10
	v_mul_f32_e32 v3, 0xbfb8aa3b, v11
	v_exp_f32_e32 v3, v3
	s_nop 0
	v_add_f32_e32 v3, 1.0, v3
	v_rcp_f32_e32 v17, v3
	s_nop 0
	v_pk_mul_f32 v[16:17], v[16:17], v[10:11]
	v_mul_f32_e32 v11, v97, v10
	v_mul_f32_e32 v3, 0xbfb8aa3b, v11
	v_exp_f32_e32 v3, v3
	s_nop 0
	v_add_f32_e32 v3, 1.0, v3
	v_rcp_f32_e32 v19, v3
	s_nop 0
	v_pk_mul_f32 v[18:19], v[18:19], v[10:11]
	v_mul_f32_e32 v11, v82, v10
	v_mul_f32_e32 v3, 0xbfb8aa3b, v11
	v_exp_f32_e32 v3, v3
	s_nop 0
	v_add_f32_e32 v3, 1.0, v3
	v_rcp_f32_e32 v21, v3
	s_nop 0
	v_pk_mul_f32 v[20:21], v[20:21], v[10:11]
	v_mul_f32_e32 v11, v83, v10
	v_mul_f32_e32 v3, 0xbfb8aa3b, v11
	v_exp_f32_e32 v3, v3
	s_nop 0
	v_add_f32_e32 v3, 1.0, v3
	v_rcp_f32_e32 v23, v3
	s_nop 0
	v_pk_mul_f32 v[22:23], v[22:23], v[10:11]
	v_mul_f32_e32 v11, v84, v10
	v_mul_f32_e32 v3, 0xbfb8aa3b, v11
	v_exp_f32_e32 v3, v3
	s_nop 0
	v_add_f32_e32 v3, 1.0, v3
	v_rcp_f32_e32 v25, v3
	v_mul_f32_e32 v3, v14, v15
	v_cvt_pk_fp8_f32 v28, v12, v3
	v_mul_f32_e32 v3, v16, v17
	v_pk_mul_f32 v[12:13], v[24:25], v[10:11]
	v_mul_f32_e32 v11, v85, v10
	v_mul_f32_e32 v14, 0xbfb8aa3b, v11
	v_exp_f32_e32 v14, v14
	v_mul_f32_e32 v15, v18, v19
	v_cvt_pk_fp8_f32 v28, v3, v15 op_sel:[0,0,1]
	v_mul_f32_e32 v3, v20, v21
	v_add_f32_e32 v14, 1.0, v14
	v_rcp_f32_e32 v27, v14
	v_mul_f32_e32 v14, v22, v23
	v_cvt_pk_fp8_f32 v29, v3, v14
	v_mul_f32_e32 v3, v12, v13
	v_pk_mul_f32 v[10:11], v[26:27], v[10:11]
	v_mov_b32_e32 v12, v74
	v_mul_f32_e32 v10, v10, v11
	v_cvt_pk_fp8_f32 v29, v3, v10 op_sel:[0,0,1]
	v_mad_i64_i32 v[10:11], s[64:65], v30, s71, v[6:7]
	v_lshl_add_u64 v[10:11], v[10:11], 0, v[4:5]
	global_store_dwordx2 v[10:11], v[28:29], off
	s_nop 0
	v_mov_b32_e32 v14, v75
	v_mov_b32_e32 v16, v76
	v_mov_b32_e32 v18, v77
	v_mov_b32_e32 v20, v70
	v_mov_b32_e32 v22, v71
	v_mov_b32_e32 v24, v72
	v_mov_b32_e32 v28, 0
	v_mov_b32_e32 v29, 0
	v_mov_b32_e32 v26, v73
	v_add_u32_e32 v30, 0x90, v2
	s_waitcnt vmcnt(6)
	v_mov_b32_e32 v3, v249
	v_mul_f32_e32 v10, 0x3d000000, v3
	v_mul_f32_e32 v11, v78, v10
	v_mul_f32_e32 v3, 0xbfb8aa3b, v11
	v_exp_f32_e32 v3, v3
	s_nop 0
	v_add_f32_e32 v3, 1.0, v3
	v_rcp_f32_e32 v13, v3
	s_nop 0
	v_pk_mul_f32 v[12:13], v[12:13], v[10:11]
	v_mul_f32_e32 v11, v79, v10
	v_mul_f32_e32 v3, 0xbfb8aa3b, v11
	v_exp_f32_e32 v3, v3
	v_mul_f32_e32 v12, v12, v13
	v_add_f32_e32 v3, 1.0, v3
	v_rcp_f32_e32 v15, v3
	s_nop 0
	v_pk_mul_f32 v[14:15], v[14:15], v[10:11]
	v_mul_f32_e32 v11, v80, v10
	v_mul_f32_e32 v3, 0xbfb8aa3b, v11
	v_exp_f32_e32 v3, v3
	s_nop 0
	v_add_f32_e32 v3, 1.0, v3
	v_rcp_f32_e32 v17, v3
	s_nop 0
	v_pk_mul_f32 v[16:17], v[16:17], v[10:11]
	v_mul_f32_e32 v11, v81, v10
	v_mul_f32_e32 v3, 0xbfb8aa3b, v11
	v_exp_f32_e32 v3, v3
	s_nop 0
	v_add_f32_e32 v3, 1.0, v3
	v_rcp_f32_e32 v19, v3
	s_nop 0
	v_pk_mul_f32 v[18:19], v[18:19], v[10:11]
	v_mul_f32_e32 v11, v66, v10
	v_mul_f32_e32 v3, 0xbfb8aa3b, v11
	v_exp_f32_e32 v3, v3
	s_nop 0
	v_add_f32_e32 v3, 1.0, v3
	v_rcp_f32_e32 v21, v3
	s_nop 0
	v_pk_mul_f32 v[20:21], v[20:21], v[10:11]
	v_mul_f32_e32 v11, v67, v10
	v_mul_f32_e32 v3, 0xbfb8aa3b, v11
	v_exp_f32_e32 v3, v3
	s_nop 0
	v_add_f32_e32 v3, 1.0, v3
	v_rcp_f32_e32 v23, v3
	s_nop 0
	v_pk_mul_f32 v[22:23], v[22:23], v[10:11]
	v_mul_f32_e32 v11, v68, v10
	v_mul_f32_e32 v3, 0xbfb8aa3b, v11
	v_exp_f32_e32 v3, v3
	s_nop 0
	v_add_f32_e32 v3, 1.0, v3
	v_rcp_f32_e32 v25, v3
	v_mul_f32_e32 v3, v14, v15
	v_cvt_pk_fp8_f32 v28, v12, v3
	v_mul_f32_e32 v3, v16, v17
	v_pk_mul_f32 v[12:13], v[24:25], v[10:11]
	v_mul_f32_e32 v11, v69, v10
	v_mul_f32_e32 v14, 0xbfb8aa3b, v11
	v_exp_f32_e32 v14, v14
	v_mul_f32_e32 v15, v18, v19
	v_cvt_pk_fp8_f32 v28, v3, v15 op_sel:[0,0,1]
	v_mul_f32_e32 v3, v20, v21
	v_add_f32_e32 v14, 1.0, v14
	v_rcp_f32_e32 v27, v14
	v_mul_f32_e32 v14, v22, v23
	v_cvt_pk_fp8_f32 v29, v3, v14
	v_mul_f32_e32 v3, v12, v13
	v_pk_mul_f32 v[10:11], v[26:27], v[10:11]
	v_mov_b32_e32 v12, v58
	v_mul_f32_e32 v10, v10, v11
	v_cvt_pk_fp8_f32 v29, v3, v10 op_sel:[0,0,1]
	v_mad_i64_i32 v[10:11], s[64:65], v30, s71, v[6:7]
	v_lshl_add_u64 v[10:11], v[10:11], 0, v[4:5]
	global_store_dwordx2 v[10:11], v[28:29], off
	s_nop 0
	v_mov_b32_e32 v14, v59
	v_mov_b32_e32 v16, v60
	v_mov_b32_e32 v18, v61
	v_mov_b32_e32 v20, v54
	v_mov_b32_e32 v22, v55
	v_mov_b32_e32 v24, v56
	v_mov_b32_e32 v28, 0
	v_mov_b32_e32 v29, 0
	v_mov_b32_e32 v26, v57
	v_add_u32_e32 v30, 0xa0, v2
	s_waitcnt vmcnt(5)
; __device__ __forceinline__ float sigm(float x) { return __builtin_amdgcn_rcpf(1.f + __builtin_amdgcn_exp2f(-1.4426950408889634f * x)); }
; __device__ __forceinline__ unsigned pk4_fp8(float a, float b, float c, float d) { int w = 0; w = __builtin_amdgcn_cvt_pk_fp8_f32(a, b, w, false); w = __builtin_amdgcn_cvt_pk_fp8_f32(c, d, w, true); return (unsigned)w; }
; __device__ __forceinline__ u32x4 pack8(f32x4 v0, f32x4 v1) { u32x4 w; w.x = cvt_pk_bf16(v0[0], v0[1]); w.y = cvt_pk_bf16(v0[2], v0[3]); w.z = cvt_pk_bf16(v1[0], v1[1]); w.w = cvt_pk_bf16(v1[2], v1[3]); return w; }
; template <class T> __device__ __forceinline__ void est(T* p, T v) { if constexpr (MK_EPI_NT != 0) __builtin_nontemporal_store(v, p); else *p = v; }
; __device__ __forceinline__ float ss_val(const ss_t* ss, int row) { return (float)ss[row] * (1.f / 16777216.f); }
;     __device__ __forceinline__ void operator()(AccT acc, const Unit& u, int wr, int wc, int fr, int fq) const {
;         const int row0 = u.pm * 256 + wr * 64 + fr, col0 = u.pn * 128 + wc * 32 + 8 * fq;
; #pragma unroll
;         for (int ai = 0; ai < 2; ++ai)
; #pragma unroll
;             for (int m = 0; m < 4; ++m) { const int row = row0 + ai * 128 + m * 16; const float r = (is_rstd ? ((const float*)rs)[row] : rsqrtf(ss_val((const ss_t*)rs, row) * (1.0f / DM) + EPS)) * ascale;
;                 f32x4 o[2];
; #pragma unroll
;                 for (int bj = 0; bj < 2; ++bj) { const f32x4 a = acc[ai][bj][m][0] * r, b = acc[ai][bj][m][1] * r;
; #pragma unroll
;                     for (int j = 0; j < 4; ++j) o[bj][j] = a[j] * sigm(a[j]) * b[j]; }
;                 if constexpr (F8OUT) est((u32x2*)((unsigned char*)O + (size_t)row * ldo + col0), (u32x2)(u32x2){pk4_fp8(o[0][0], o[0][1], o[0][2], o[0][3]), pk4_fp8(o[1][0], o[1][1], o[1][2], o[1][3])});
;                 else est((u32x4*)((bf16_t*)O + (size_t)row * ldo + col0), (u32x4)pack8(o[0], o[1])); }
	v_mov_b32_e32 v3, v250
	v_mul_f32_e32 v10, 0x3d000000, v3
	v_mul_f32_e32 v11, v62, v10
	v_mul_f32_e32 v3, 0xbfb8aa3b, v11
	v_exp_f32_e32 v3, v3
	s_nop 0
	v_add_f32_e32 v3, 1.0, v3
	v_rcp_f32_e32 v13, v3
	s_nop 0
	v_pk_mul_f32 v[12:13], v[12:13], v[10:11]
	v_mul_f32_e32 v11, v63, v10
	v_mul_f32_e32 v3, 0xbfb8aa3b, v11
	v_exp_f32_e32 v3, v3
	v_mul_f32_e32 v12, v12, v13
	v_add_f32_e32 v3, 1.0, v3
	v_rcp_f32_e32 v15, v3
	s_nop 0
	v_pk_mul_f32 v[14:15], v[14:15], v[10:11]
	v_mul_f32_e32 v11, v64, v10
	v_mul_f32_e32 v3, 0xbfb8aa3b, v11
	v_exp_f32_e32 v3, v3
	s_nop 0
	v_add_f32_e32 v3, 1.0, v3
	v_rcp_f32_e32 v17, v3
	s_nop 0
	v_pk_mul_f32 v[16:17], v[16:17], v[10:11]
	v_mul_f32_e32 v11, v65, v10
	v_mul_f32_e32 v3, 0xbfb8aa3b, v11
	v_exp_f32_e32 v3, v3
	s_nop 0
	v_add_f32_e32 v3, 1.0, v3
	v_rcp_f32_e32 v19, v3
	s_nop 0
	v_pk_mul_f32 v[18:19], v[18:19], v[10:11]
	v_mul_f32_e32 v11, v50, v10
	v_mul_f32_e32 v3, 0xbfb8aa3b, v11
	v_exp_f32_e32 v3, v3
	s_nop 0
	v_add_f32_e32 v3, 1.0, v3
	v_rcp_f32_e32 v21, v3
	s_nop 0
	v_pk_mul_f32 v[20:21], v[20:21], v[10:11]
	v_mul_f32_e32 v11, v51, v10
	v_mul_f32_e32 v3, 0xbfb8aa3b, v11
	v_exp_f32_e32 v3, v3
	s_nop 0
	v_add_f32_e32 v3, 1.0, v3
	v_rcp_f32_e32 v23, v3
	s_nop 0
	v_pk_mul_f32 v[22:23], v[22:23], v[10:11]
	v_mul_f32_e32 v11, v52, v10
	v_mul_f32_e32 v3, 0xbfb8aa3b, v11
	v_exp_f32_e32 v3, v3
	s_nop 0
	v_add_f32_e32 v3, 1.0, v3
	v_rcp_f32_e32 v25, v3
	v_mul_f32_e32 v3, v14, v15
	v_cvt_pk_fp8_f32 v28, v12, v3
	v_mul_f32_e32 v3, v16, v17
	v_pk_mul_f32 v[12:13], v[24:25], v[10:11]
	v_mul_f32_e32 v11, v53, v10
	v_mul_f32_e32 v14, 0xbfb8aa3b, v11
	v_exp_f32_e32 v14, v14
	v_mul_f32_e32 v15, v18, v19
	v_cvt_pk_fp8_f32 v28, v3, v15 op_sel:[0,0,1]
	v_mul_f32_e32 v3, v20, v21
	v_add_f32_e32 v14, 1.0, v14
	v_rcp_f32_e32 v27, v14
	v_mul_f32_e32 v14, v22, v23
	v_cvt_pk_fp8_f32 v29, v3, v14
	v_mul_f32_e32 v3, v12, v13
	v_pk_mul_f32 v[10:11], v[26:27], v[10:11]
	v_mov_b32_e32 v12, v43
	v_mul_f32_e32 v10, v10, v11
	v_cvt_pk_fp8_f32 v29, v3, v10 op_sel:[0,0,1]
	v_mad_i64_i32 v[10:11], s[64:65], v30, s71, v[6:7]
	v_lshl_add_u64 v[10:11], v[10:11], 0, v[4:5]
	global_store_dwordx2 v[10:11], v[28:29], off
	s_nop 0
	v_mov_b32_e32 v10, v42
	v_mov_b32_e32 v14, v44
	v_mov_b32_e32 v16, v45
	v_mov_b32_e32 v18, v38
	v_mov_b32_e32 v20, v39
	v_mov_b32_e32 v22, v40
	v_mov_b32_e32 v26, 0
	v_add_u32_e32 v28, 0xb0, v2
	v_mov_b32_e32 v27, 0
	v_mov_b32_e32 v24, v41
	s_waitcnt vmcnt(4)
	v_mov_b32_e32 v3, v251
	v_mul_f32_e32 v8, 0x3d000000, v3
	v_mul_f32_e32 v9, v46, v8
	v_mul_f32_e32 v3, 0xbfb8aa3b, v9
	v_exp_f32_e32 v3, v3
	s_nop 0
	v_add_f32_e32 v3, 1.0, v3
	v_rcp_f32_e32 v11, v3
	s_nop 0
	v_pk_mul_f32 v[10:11], v[10:11], v[8:9]
	v_mul_f32_e32 v9, v47, v8
	v_mul_f32_e32 v3, 0xbfb8aa3b, v9
	v_exp_f32_e32 v3, v3
	v_mul_f32_e32 v2, v10, v11
	v_add_f32_e32 v3, 1.0, v3
	v_rcp_f32_e32 v13, v3
	s_nop 0
	v_pk_mul_f32 v[12:13], v[12:13], v[8:9]
	v_mul_f32_e32 v9, v48, v8
	v_mul_f32_e32 v3, 0xbfb8aa3b, v9
	v_exp_f32_e32 v3, v3
	s_nop 0
	v_add_f32_e32 v3, 1.0, v3
	v_rcp_f32_e32 v15, v3
	s_nop 0
	v_pk_mul_f32 v[14:15], v[14:15], v[8:9]
	v_mul_f32_e32 v9, v49, v8
	v_mul_f32_e32 v3, 0xbfb8aa3b, v9
	v_exp_f32_e32 v3, v3
	v_mul_f32_e32 v10, v14, v15
	v_add_f32_e32 v3, 1.0, v3
	v_rcp_f32_e32 v17, v3
	s_nop 0
	v_pk_mul_f32 v[16:17], v[16:17], v[8:9]
	v_mul_f32_e32 v9, v34, v8
	v_mul_f32_e32 v3, 0xbfb8aa3b, v9
	v_exp_f32_e32 v3, v3
	s_nop 0
	v_add_f32_e32 v3, 1.0, v3
	v_rcp_f32_e32 v19, v3
	s_nop 0
	v_pk_mul_f32 v[18:19], v[18:19], v[8:9]
	v_mul_f32_e32 v9, v35, v8
	v_mul_f32_e32 v3, 0xbfb8aa3b, v9
	v_exp_f32_e32 v3, v3
	s_nop 0
	v_add_f32_e32 v3, 1.0, v3
	v_rcp_f32_e32 v21, v3
	s_nop 0
	v_pk_mul_f32 v[20:21], v[20:21], v[8:9]
	v_mul_f32_e32 v9, v36, v8
	v_mul_f32_e32 v3, 0xbfb8aa3b, v9
	v_exp_f32_e32 v3, v3
	s_nop 0
	v_add_f32_e32 v3, 1.0, v3
	v_rcp_f32_e32 v23, v3
	v_mul_f32_e32 v3, v12, v13
	v_cvt_pk_fp8_f32 v26, v2, v3
	v_mul_f32_e32 v12, v16, v17
	v_pk_mul_f32 v[2:3], v[22:23], v[8:9]
	v_mul_f32_e32 v9, v37, v8
	v_mul_f32_e32 v11, 0xbfb8aa3b, v9
	v_exp_f32_e32 v11, v11
	v_cvt_pk_fp8_f32 v26, v10, v12 op_sel:[0,0,1]
	v_mul_f32_e32 v10, v18, v19
	v_add_f32_e32 v11, 1.0, v11
	v_rcp_f32_e32 v25, v11
	v_mul_f32_e32 v11, v20, v21
	v_cvt_pk_fp8_f32 v27, v10, v11
	v_mul_f32_e32 v10, v2, v3
	v_pk_mul_f32 v[2:3], v[24:25], v[8:9]
	s_nop 0
	v_mul_f32_e32 v2, v2, v3
	v_cvt_pk_fp8_f32 v27, v10, v2 op_sel:[0,0,1]
	v_mad_i64_i32 v[2:3], s[64:65], v28, s71, v[6:7]
	v_lshl_add_u64 v[2:3], v[2:3], 0, v[4:5]
	global_store_dwordx2 v[2:3], v[26:27], off
	s_cbranch_vccnz .LBB0_2254
	s_andn2_b64 vcc, exec, s[22:23]
	s_cbranch_vccnz .LBB0_2253
	s_barrier
	s_branch .LBB0_2253
